# row-pass wave sums: the xor-16 step through v_permlane16_swap instead of the last ds_swizzle round trip (same code size, bit-identical sums)
# baseline (speedup 1.0000x reference)
; #define RP_UNPK(V_, H_) ((H_) ? (f32x4){bflo((V_)[2]), bfhi((V_)[2]), bflo((V_)[3]), bfhi((V_)[3])} : (f32x4){bflo((V_)[0]), bfhi((V_)[0]), bflo((V_)[1]), bfhi((V_)[1])})
; template <int MODE, bool FIRSTX>
; __device__ __forceinline__ void row_pass(Frame& F, int layer, bool final_out, int row0) {
;     ...
;         f32x4 v[4];
; #pragma unroll
;         for (int q = 0; q < 4; ++q) v[q] = FIRSTX ? xf[q] : RP_UNPK(xb[q >> 1], q & 1);
;         if (MODE != 0) {
; #pragma unroll
;             for (int q = 0; q < 4; ++q) { f32x4 y = (f32x4){0.f, 0.f, 0.f, 0.f};
; #pragma unroll
;                 for (int k = 0; k < NY; ++k) { if (MODE == 2) { const unsigned w8 = yb[k][q >> 1][q & 1]; const f32x2 lo = __builtin_amdgcn_cvt_pk_f32_fp8((int)w8, false), hi = __builtin_amdgcn_cvt_pk_f32_fp8((int)w8, true); y += (f32x4){lo.x, lo.y, hi.x, hi.y}; }
;                                                 else y += RP_UNPK(yb[k][q >> 1], q & 1); }
;                 if (MODE == 2) y = y * (1.0f / YK8_SCALE);
;                 v[q] = v[q] * DN_ALPHA + gt[q] * y; }
;             float s = 0.f;
; #pragma unroll
;             for (int q = 0; q < 4; ++q) s += (v[q][0] + v[q][1]) + (v[q][2] + v[q][3]);
;             const float mean = wave_sum(s) * (1.0f / DM); float qq = 0.f;
; #pragma unroll
;             for (int q = 0; q < 4; ++q) { v[q] = v[q] - mean; qq += (v[q][0] * v[q][0] + v[q][1] * v[q][1]) + (v[q][2] * v[q][2] + v[q][3] * v[q][3]); }
;             const float rstd = 1.0f / sqrtf(wave_sum(qq) * (1.0f / DM) + LN_EPS);
.Lrp1_common:
	v_lshlrev_b32_e32 v128, 16, v102
	v_and_b32_e32 v129, 0xffff0000, v102
	v_lshlrev_b32_e32 v102, 16, v103
	v_and_b32_e32 v103, 0xffff0000, v103
	v_pk_add_f32 v[102:103], v[102:103], 0 op_sel_hi:[1,0]
	v_pk_add_f32 v[128:129], v[128:129], 0 op_sel_hi:[1,0]
	v_lshlrev_b32_e32 v120, 16, v110
	v_and_b32_e32 v121, 0xffff0000, v110
	v_lshlrev_b32_e32 v110, 16, v111
	v_and_b32_e32 v111, 0xffff0000, v111
	v_pk_mul_f32 v[128:129], v[128:129], v[46:47]
	v_pk_mul_f32 v[102:103], v[102:103], v[48:49]
	v_lshlrev_b32_e32 v122, 16, v112
	v_pk_fma_f32 v[102:103], v[110:111], s[62:63], v[102:103] op_sel_hi:[1,0,1]
	v_pk_fma_f32 v[110:111], v[120:121], s[62:63], v[128:129] op_sel_hi:[1,0,1]
	v_lshlrev_b32_e32 v120, 16, v104
	v_and_b32_e32 v121, 0xffff0000, v104
	v_lshlrev_b32_e32 v104, 16, v105
	v_and_b32_e32 v105, 0xffff0000, v105
	v_pk_add_f32 v[104:105], v[104:105], 0 op_sel_hi:[1,0]
	v_pk_add_f32 v[120:121], v[120:121], 0 op_sel_hi:[1,0]
	v_and_b32_e32 v123, 0xffff0000, v112
	v_lshlrev_b32_e32 v112, 16, v113
	v_and_b32_e32 v113, 0xffff0000, v113
	v_pk_mul_f32 v[120:121], v[120:121], v[42:43]
	v_pk_mul_f32 v[104:105], v[104:105], v[44:45]
	v_lshlrev_b32_e32 v124, 16, v106
	v_pk_fma_f32 v[104:105], v[112:113], s[62:63], v[104:105] op_sel_hi:[1,0,1]
	v_pk_fma_f32 v[112:113], v[122:123], s[62:63], v[120:121] op_sel_hi:[1,0,1]
	v_lshlrev_b32_e32 v120, 16, v98
	v_and_b32_e32 v121, 0xffff0000, v98
	v_lshlrev_b32_e32 v98, 16, v99
	v_and_b32_e32 v99, 0xffff0000, v99
	v_pk_add_f32 v[98:99], v[98:99], 0 op_sel_hi:[1,0]
	v_pk_add_f32 v[120:121], v[120:121], 0 op_sel_hi:[1,0]
	v_and_b32_e32 v125, 0xffff0000, v106
	v_lshlrev_b32_e32 v106, 16, v107
	v_and_b32_e32 v107, 0xffff0000, v107
	v_pk_mul_f32 v[120:121], v[120:121], v[78:79]
	v_pk_mul_f32 v[98:99], v[98:99], v[80:81]
	v_lshlrev_b32_e32 v126, 16, v108
	v_pk_fma_f32 v[98:99], v[106:107], s[62:63], v[98:99] op_sel_hi:[1,0,1]
	v_pk_fma_f32 v[106:107], v[124:125], s[62:63], v[120:121] op_sel_hi:[1,0,1]
	v_lshlrev_b32_e32 v120, 16, v100
	v_and_b32_e32 v121, 0xffff0000, v100
	v_lshlrev_b32_e32 v100, 16, v101
	v_and_b32_e32 v101, 0xffff0000, v101
	v_pk_add_f32 v[100:101], v[100:101], 0 op_sel_hi:[1,0]
	v_pk_add_f32 v[120:121], v[120:121], 0 op_sel_hi:[1,0]
	v_and_b32_e32 v127, 0xffff0000, v108
	v_lshlrev_b32_e32 v108, 16, v109
	v_and_b32_e32 v109, 0xffff0000, v109
	v_pk_mul_f32 v[120:121], v[120:121], v[70:71]
	v_pk_mul_f32 v[100:101], v[100:101], v[72:73]
	v_add_f32_e32 v122, v104, v105
	v_pk_fma_f32 v[100:101], v[108:109], s[62:63], v[100:101] op_sel_hi:[1,0,1]
	v_pk_fma_f32 v[108:109], v[126:127], s[62:63], v[120:121] op_sel_hi:[1,0,1]
	v_add_f32_e32 v120, v110, v111
	v_add_f32_e32 v121, v102, v103
	v_add_f32_e32 v120, v120, v121
	v_add_f32_e32 v121, v112, v113
	v_add_f32_e32 v120, 0, v120
	v_add_f32_e32 v121, v121, v122
	v_add_f32_e32 v120, v121, v120
	v_add_f32_e32 v121, v106, v107
	v_add_f32_e32 v122, v98, v99
	v_add_f32_e32 v121, v121, v122
	v_add_f32_e32 v120, v121, v120
	v_add_f32_e32 v121, v108, v109
	v_add_f32_e32 v122, v100, v101
	v_add_f32_e32 v121, v121, v122
	v_add_f32_e32 v120, v121, v120
	s_nop 1
	v_add_f32_dpp v120, v120, v120 quad_perm:[1,0,3,2] row_mask:0xf bank_mask:0xf
	s_add_i32 s11, s11, 1
	v_lshl_add_u64 v[118:119], v[118:119], 0, s[50:51]
	s_cmp_lt_i32 s1, s14
	s_nop 1
	v_add_f32_dpp v120, v120, v120 quad_perm:[2,3,0,1] row_mask:0xf bank_mask:0xf
	s_nop 1
	v_add_f32_dpp v120, v120, v120 row_half_mirror row_mask:0xf bank_mask:0xf
	s_nop 1
	v_add_f32_dpp v120, v120, v120 row_mirror row_mask:0xf bank_mask:0xf
	s_waitcnt lgkmcnt(0)
	v_mov_b32_e32 v121, v120
	s_nop 1
	v_permlane16_swap_b32_e32 v120, v121
	v_add_f32_e32 v120, v120, v121
	v_mov_b32_e32 v121, v120
	s_nop 1
	v_permlane32_swap_b32_e32 v120, v121
	v_add_f32_e32 v120, v120, v121
	v_fmac_f32_e32 v103, 0xba800000, v120
	v_fmac_f32_e32 v111, 0xba800000, v120
	v_fmamk_f32 v102, v120, 0xba800000, v102
	v_fmamk_f32 v110, v120, 0xba800000, v110
	v_mul_f32_e32 v121, v111, v111
	v_mul_f32_e32 v122, v103, v103
	v_fmac_f32_e32 v121, v110, v110
	v_fmac_f32_e32 v122, v102, v102
	v_fmac_f32_e32 v105, 0xba800000, v120
	v_fmac_f32_e32 v113, 0xba800000, v120
	v_add_f32_e32 v121, v121, v122
	v_fmamk_f32 v104, v120, 0xba800000, v104
	v_fmamk_f32 v112, v120, 0xba800000, v112
	v_mul_f32_e32 v122, v113, v113
	v_mul_f32_e32 v123, v105, v105
	v_fmac_f32_e32 v122, v112, v112
	v_fmac_f32_e32 v123, v104, v104
	v_add_f32_e32 v122, v122, v123
	v_fmac_f32_e32 v99, 0xba800000, v120
	v_fmac_f32_e32 v107, 0xba800000, v120
	v_add_f32_e32 v121, v121, v122
	v_fmamk_f32 v98, v120, 0xba800000, v98
	v_fmamk_f32 v106, v120, 0xba800000, v106
	v_mul_f32_e32 v122, v107, v107
	v_mul_f32_e32 v123, v99, v99
	v_fmac_f32_e32 v122, v106, v106
	v_fmac_f32_e32 v123, v98, v98
	v_add_f32_e32 v122, v122, v123
	v_fmac_f32_e32 v101, 0xba800000, v120
	v_fmac_f32_e32 v109, 0xba800000, v120
	v_add_f32_e32 v121, v122, v121
	v_fmamk_f32 v100, v120, 0xba800000, v100
	v_fmamk_f32 v108, v120, 0xba800000, v108
	v_mul_f32_e32 v120, v109, v109
	v_mul_f32_e32 v122, v101, v101
	v_fmac_f32_e32 v120, v108, v108
	v_fmac_f32_e32 v122, v100, v100
	v_add_f32_e32 v120, v120, v122
	v_add_f32_e32 v120, v120, v121
	s_nop 1
	v_add_f32_dpp v120, v120, v120 quad_perm:[1,0,3,2] row_mask:0xf bank_mask:0xf
	s_nop 1
	v_add_f32_dpp v120, v120, v120 quad_perm:[2,3,0,1] row_mask:0xf bank_mask:0xf
	s_nop 1
	v_add_f32_dpp v120, v120, v120 row_half_mirror row_mask:0xf bank_mask:0xf
	s_nop 1
	v_add_f32_dpp v120, v120, v120 row_mirror row_mask:0xf bank_mask:0xf
	s_waitcnt lgkmcnt(0)
; __device__ __forceinline__ unsigned pk2(float lo, float hi) { return f2bf(lo) | (f2bf(hi) << 16); }
; __device__ __forceinline__ unsigned cvt_fp8x4(float a, float b, float c, float d) { int w = __builtin_amdgcn_cvt_pk_fp8_f32(a, b, 0, false); w = __builtin_amdgcn_cvt_pk_fp8_f32(c, d, w, true); return (unsigned)w; }
; template <int MODE, bool FIRSTX>
; __device__ __forceinline__ void row_pass(Frame& F, int layer, bool final_out, int row0) {
;     ...
;             const float rstd = 1.0f / sqrtf(wave_sum(qq) * (1.0f / DM) + LN_EPS);
; #pragma unroll
;             for (int q = 0; q < 4; ++q) v[q] = v[q] * rstd * lg[q] + lb[q];
;             if (final_out) { if (row >= NCTX) {
; #pragma unroll
;                 for (int q = 0; q < 4; ++q) *(f32x4*)(F.out + (size_t)(row - NCTX) * DM + RP_COL(q)) = v[q]; } }
;             else {
; #pragma unroll
;                 for (int j = 0; j < 2; ++j) { u32x4 w; w.x = pk2(v[2 * j][0], v[2 * j][1]); w.y = pk2(v[2 * j][2], v[2 * j][3]); w.z = pk2(v[2 * j + 1][0], v[2 * j + 1][1]); w.w = pk2(v[2 * j + 1][2], v[2 * j + 1][3]);
;                     *(u32x4*)(X + (size_t)row * DM + lc + 512 * j) = w; } }
;         }
;         if (!final_out) {
; #pragma unroll
;             for (int j = 0; j < 2; ++j) { const f32x4 h0 = v[2 * j] * (sc[2 * j] + 1.0f) + sh[2 * j], h1 = v[2 * j + 1] * (sc[2 * j + 1] + 1.0f) + sh[2 * j + 1];
;                 if (MODE == 1 || (nlayer % 3) == 2) { u32x4 w; w.x = pk2(h0[0], h0[1]); w.y = pk2(h0[2], h0[3]); w.z = pk2(h1[0], h1[1]); w.w = pk2(h1[2], h1[3]);
;                     *(u32x4*)(H + (size_t)row * DM + lc + 512 * j) = w; }
;                 if (MODE == 1 || (nlayer % 3) != 2) {                                u32x2 w8; w8.x = cvt_fp8x4(h0[0], h0[1], h0[2], h0[3]); w8.y = cvt_fp8x4(h1[0], h1[1], h1[2], h1[3]); *(u32x2*)(F.ws + WS_H8 + (size_t)row * DM + lc + 512 * j) = w8; } }
	v_mov_b32_e32 v121, v120
	s_nop 1
	v_permlane16_swap_b32_e32 v120, v121
	v_add_f32_e32 v120, v120, v121
	v_mov_b32_e32 v121, v120
	s_nop 1
	v_permlane32_swap_b32_e32 v120, v121
	v_add_f32_e32 v120, v120, v121
	v_fmamk_f32 v120, v120, 0x3a800000, v188
	v_mul_f32_e32 v121, 0x4f800000, v120
	v_cmp_gt_f32_e32 vcc, s31, v120
	s_nop 1
	v_cndmask_b32_e32 v120, v120, v121, vcc
	v_sqrt_f32_e32 v121, v120
	s_nop 0
	v_add_u32_e32 v122, -1, v121
	v_fma_f32 v123, -v122, v121, v120
	v_cmp_ge_f32_e64 s[2:3], 0, v123
	v_add_u32_e32 v123, 1, v121
	s_nop 0
	v_cndmask_b32_e64 v122, v121, v122, s[2:3]
	v_fma_f32 v121, -v123, v121, v120
	v_cmp_lt_f32_e64 s[2:3], 0, v121
	s_nop 1
	v_cndmask_b32_e64 v121, v122, v123, s[2:3]
	v_mul_f32_e32 v122, 0x37800000, v121
	v_cndmask_b32_e32 v121, v121, v122, vcc
	v_cmp_class_f32_e32 vcc, v120, v189
	s_nop 1
	v_cndmask_b32_e32 v120, v121, v120, vcc
	v_div_scale_f32 v121, s[2:3], v120, v120, 1.0
	v_rcp_f32_e32 v122, v121
	s_nop 0
	v_fma_f32 v123, -v121, v122, 1.0
	v_fmac_f32_e32 v122, v123, v122
	v_div_scale_f32 v123, vcc, 1.0, v120, 1.0
	v_mul_f32_e32 v124, v123, v122
	v_fma_f32 v125, -v121, v124, v123
	v_fmac_f32_e32 v124, v125, v122
	v_fma_f32 v121, -v121, v124, v123
	v_div_fmas_f32 v121, v121, v122, v124
	v_div_fixup_f32 v120, v121, v120, 1.0
	v_pk_mul_f32 v[110:111], v[110:111], v[120:121] op_sel_hi:[1,0]
	v_pk_mul_f32 v[98:99], v[98:99], v[120:121] op_sel_hi:[1,0]
	v_pk_fma_f32 v[110:111], v[2:3], v[110:111], v[6:7]
	v_pk_fma_f32 v[122:123], v[20:21], v[98:99], v[24:25]
	v_pk_mul_f32 v[98:99], v[100:101], v[120:121] op_sel_hi:[1,0]
	v_pk_mul_f32 v[102:103], v[102:103], v[120:121] op_sel_hi:[1,0]
	v_pk_mul_f32 v[112:113], v[112:113], v[120:121] op_sel_hi:[1,0]
	v_pk_mul_f32 v[104:105], v[104:105], v[120:121] op_sel_hi:[1,0]
	v_pk_mul_f32 v[106:107], v[106:107], v[120:121] op_sel_hi:[1,0]
	v_pk_mul_f32 v[100:101], v[108:109], v[120:121] op_sel_hi:[1,0]
	v_pk_fma_f32 v[120:121], v[28:29], v[98:99], v[32:33]
	v_bfe_u32 v98, v110, 16, 1
	v_add3_u32 v98, v110, v98, s43
	v_bfe_u32 v99, v111, 16, 1
	v_pk_fma_f32 v[102:103], v[4:5], v[102:103], v[8:9]
	v_lshrrev_b32_e32 v98, 16, v98
	v_add3_u32 v99, v111, v99, s43
	v_and_or_b32 v98, v99, s33, v98
	v_bfe_u32 v99, v102, 16, 1
	v_pk_fma_f32 v[108:109], v[26:27], v[100:101], v[30:31]
	v_add3_u32 v99, v102, v99, s43
	v_bfe_u32 v100, v103, 16, 1
	v_pk_fma_f32 v[112:113], v[10:11], v[112:113], v[14:15]
	v_lshrrev_b32_e32 v99, 16, v99
	v_add3_u32 v100, v103, v100, s43
	v_and_or_b32 v99, v100, s33, v99
	v_bfe_u32 v100, v112, 16, 1
	v_add3_u32 v100, v112, v100, s43
	v_bfe_u32 v101, v113, 16, 1
	v_pk_fma_f32 v[104:105], v[12:13], v[104:105], v[16:17]
	v_lshrrev_b32_e32 v100, 16, v100
	v_add3_u32 v101, v113, v101, s43
	v_and_or_b32 v100, v101, s33, v100
	v_bfe_u32 v101, v104, 16, 1
	v_add3_u32 v101, v104, v101, s43
	v_bfe_u32 v126, v105, 16, 1
	v_lshl_add_u64 v[124:125], s[74:75], 0, v[114:115]
	v_lshrrev_b32_e32 v101, 16, v101
	v_add3_u32 v126, v105, v126, s43
	v_and_or_b32 v101, v126, s33, v101
	v_add_co_u32_e32 v126, vcc, s39, v124
	v_pk_fma_f32 v[106:107], v[18:19], v[106:107], v[22:23]
	s_nop 0
	v_addc_co_u32_e32 v127, vcc, 0, v125, vcc
	global_store_dwordx4 v[126:127], v[98:101], off
	v_bfe_u32 v128, v121, 16, 1
	v_add3_u32 v128, v121, v128, s43
	v_bfe_u32 v98, v106, 16, 1
	v_add3_u32 v98, v106, v98, s43
	v_bfe_u32 v99, v107, 16, 1
	v_lshrrev_b32_e32 v98, 16, v98
	v_add3_u32 v99, v107, v99, s43
	v_and_or_b32 v98, v99, s33, v98
	v_bfe_u32 v99, v122, 16, 1
	v_add3_u32 v99, v122, v99, s43
	v_bfe_u32 v100, v123, 16, 1
	v_lshrrev_b32_e32 v99, 16, v99
	v_add3_u32 v100, v123, v100, s43
	v_and_or_b32 v99, v100, s33, v99
	v_bfe_u32 v100, v108, 16, 1
	v_add3_u32 v100, v108, v100, s43
	v_bfe_u32 v101, v109, 16, 1
	v_lshrrev_b32_e32 v100, 16, v100
	v_add3_u32 v101, v109, v101, s43
	v_and_or_b32 v100, v101, s33, v100
	v_bfe_u32 v101, v120, 16, 1
	v_add3_u32 v101, v120, v101, s43
	v_lshrrev_b32_e32 v101, 16, v101
	v_and_or_b32 v101, v128, s33, v101
	global_store_dwordx4 v[126:127], v[98:101], off offset:1024
	v_lshl_add_u64 v[114:115], v[114:115], 0, s[50:51]
	s_nop 0
	v_pk_add_f32 v[98:99], v[76:77], 1.0 op_sel_hi:[1,0]
	v_pk_add_f32 v[100:101], v[74:75], 1.0 op_sel_hi:[1,0]
	v_pk_fma_f32 v[102:103], v[98:99], v[102:103], v[64:65]
	v_pk_fma_f32 v[110:111], v[100:101], v[110:111], v[62:63]
	v_pk_add_f32 v[98:99], v[68:69], 1.0 op_sel_hi:[1,0]
	v_pk_add_f32 v[100:101], v[66:67], 1.0 op_sel_hi:[1,0]
	v_pk_fma_f32 v[104:105], v[98:99], v[104:105], v[60:61]
	v_and_b32_sdwa v99, v110, v185 dst_sel:DWORD dst_unused:UNUSED_PAD src0_sel:WORD_1 src1_sel:DWORD
	v_pk_fma_f32 v[112:113], v[100:101], v[112:113], v[58:59]
	v_add3_u32 v100, v110, v99, s43
	v_and_b32_sdwa v99, v103, v185 dst_sel:DWORD dst_unused:UNUSED_PAD src0_sel:WORD_1 src1_sel:DWORD
; __device__ __forceinline__ unsigned pk2(float lo, float hi) { return f2bf(lo) | (f2bf(hi) << 16); }
; __device__ __forceinline__ unsigned cvt_fp8x4(float a, float b, float c, float d) { int w = __builtin_amdgcn_cvt_pk_fp8_f32(a, b, 0, false); w = __builtin_amdgcn_cvt_pk_fp8_f32(c, d, w, true); return (unsigned)w; }
; template <int MODE, bool FIRSTX>
; __device__ __forceinline__ void row_pass(Frame& F, int layer, bool final_out, int row0) {
;     ...
;         if (!final_out) {
; #pragma unroll
;             for (int j = 0; j < 2; ++j) { const f32x4 h0 = v[2 * j] * (sc[2 * j] + 1.0f) + sh[2 * j], h1 = v[2 * j + 1] * (sc[2 * j + 1] + 1.0f) + sh[2 * j + 1];
;                 if (MODE == 1 || (nlayer % 3) == 2) { u32x4 w; w.x = pk2(h0[0], h0[1]); w.y = pk2(h0[2], h0[3]); w.z = pk2(h1[0], h1[1]); w.w = pk2(h1[2], h1[3]);
;                     *(u32x4*)(H + (size_t)row * DM + lc + 512 * j) = w; }
;                 if (MODE == 1 || (nlayer % 3) != 2) {                                u32x2 w8; w8.x = cvt_fp8x4(h0[0], h0[1], h0[2], h0[3]); w8.y = cvt_fp8x4(h1[0], h1[1], h1[2], h1[3]); *(u32x2*)(F.ws + WS_H8 + (size_t)row * DM + lc + 512 * j) = w8; } }
;         }
; #pragma unroll
;         for (int q = 0; q < 4; ++q) xf[q] = xfn[q];
; #pragma unroll
;         for (int j = 0; j < 2; ++j) { xb[j] = xbn[j];
; #pragma unroll
;             for (int k = 0; k < (NY ? NY : 1); ++k) yb[k][j] = ybn[k][j]; }
	v_and_b32_sdwa v101, v111, v185 dst_sel:DWORD dst_unused:UNUSED_PAD src0_sel:WORD_1 src1_sel:DWORD
	v_and_b32_sdwa v98, v102, v185 dst_sel:DWORD dst_unused:UNUSED_PAD src0_sel:WORD_1 src1_sel:DWORD
	v_add3_u32 v99, v103, v99, s43
	v_add3_u32 v101, v111, v101, s43
	v_add3_u32 v98, v102, v98, s43
	v_and_b32_e32 v99, 0xffff0000, v99
	v_and_b32_e32 v101, 0xffff0000, v101
	v_or_b32_sdwa v99, v99, v98 dst_sel:DWORD dst_unused:UNUSED_PAD src0_sel:DWORD src1_sel:WORD_1
	v_or_b32_sdwa v98, v101, v100 dst_sel:DWORD dst_unused:UNUSED_PAD src0_sel:DWORD src1_sel:WORD_1
	v_and_b32_sdwa v101, v112, v185 dst_sel:DWORD dst_unused:UNUSED_PAD src0_sel:WORD_1 src1_sel:DWORD
	v_add3_u32 v126, v112, v101, s43
	v_and_b32_sdwa v101, v105, v185 dst_sel:DWORD dst_unused:UNUSED_PAD src0_sel:WORD_1 src1_sel:DWORD
	v_and_b32_sdwa v127, v113, v185 dst_sel:DWORD dst_unused:UNUSED_PAD src0_sel:WORD_1 src1_sel:DWORD
	v_and_b32_sdwa v100, v104, v185 dst_sel:DWORD dst_unused:UNUSED_PAD src0_sel:WORD_1 src1_sel:DWORD
	v_add3_u32 v101, v105, v101, s43
	v_add3_u32 v127, v113, v127, s43
	v_add3_u32 v100, v104, v100, s43
	v_and_b32_e32 v101, 0xffff0000, v101
	v_and_b32_e32 v127, 0xffff0000, v127
	v_or_b32_sdwa v101, v101, v100 dst_sel:DWORD dst_unused:UNUSED_PAD src0_sel:DWORD src1_sel:WORD_1
	v_or_b32_sdwa v100, v127, v126 dst_sel:DWORD dst_unused:UNUSED_PAD src0_sel:DWORD src1_sel:WORD_1
	v_mov_b32_e32 v126, v1
	v_cvt_pk_fp8_f32 v126, v110, v111
	v_mov_b32_e32 v127, v1
	v_add_co_u32_e32 v110, vcc, s28, v124
	v_cvt_pk_fp8_f32 v127, v112, v113
	s_nop 0
	v_addc_co_u32_e32 v111, vcc, 0, v125, vcc
	global_store_dwordx4 v[110:111], v[98:101], off
	v_cvt_pk_fp8_f32 v126, v102, v103 op_sel:[0,0,1]
	v_cvt_pk_fp8_f32 v127, v104, v105 op_sel:[0,0,1]
	v_lshl_add_u64 v[98:99], s[74:75], 0, v[116:117]
	v_add_co_u32_e32 v102, vcc, s38, v98
	v_pk_add_f32 v[100:101], v[94:95], 1.0 op_sel_hi:[1,0]
	s_nop 0
	v_addc_co_u32_e32 v103, vcc, 0, v99, vcc
	v_pk_add_f32 v[98:99], v[96:97], 1.0 op_sel_hi:[1,0]
	v_pk_fma_f32 v[100:101], v[100:101], v[106:107], v[86:87]
	v_pk_fma_f32 v[104:105], v[98:99], v[122:123], v[88:89]
	v_pk_add_f32 v[98:99], v[92:93], 1.0 op_sel_hi:[1,0]
	v_pk_add_f32 v[106:107], v[90:91], 1.0 op_sel_hi:[1,0]
	v_pk_fma_f32 v[112:113], v[98:99], v[120:121], v[84:85]
	v_and_b32_sdwa v99, v100, v185 dst_sel:DWORD dst_unused:UNUSED_PAD src0_sel:WORD_1 src1_sel:DWORD
	v_pk_fma_f32 v[106:107], v[106:107], v[108:109], v[82:83]
	v_add3_u32 v108, v100, v99, s43
	v_and_b32_sdwa v99, v105, v185 dst_sel:DWORD dst_unused:UNUSED_PAD src0_sel:WORD_1 src1_sel:DWORD
	v_and_b32_sdwa v109, v101, v185 dst_sel:DWORD dst_unused:UNUSED_PAD src0_sel:WORD_1 src1_sel:DWORD
	v_and_b32_sdwa v98, v104, v185 dst_sel:DWORD dst_unused:UNUSED_PAD src0_sel:WORD_1 src1_sel:DWORD
	v_add3_u32 v99, v105, v99, s43
	v_add3_u32 v109, v101, v109, s43
	v_add3_u32 v98, v104, v98, s43
	v_and_b32_e32 v99, 0xffff0000, v99
	v_and_b32_e32 v109, 0xffff0000, v109
	v_or_b32_sdwa v99, v99, v98 dst_sel:DWORD dst_unused:UNUSED_PAD src0_sel:DWORD src1_sel:WORD_1
	v_or_b32_sdwa v98, v109, v108 dst_sel:DWORD dst_unused:UNUSED_PAD src0_sel:DWORD src1_sel:WORD_1
	v_and_b32_sdwa v108, v112, v185 dst_sel:DWORD dst_unused:UNUSED_PAD src0_sel:WORD_1 src1_sel:DWORD
	v_and_b32_sdwa v109, v106, v185 dst_sel:DWORD dst_unused:UNUSED_PAD src0_sel:WORD_1 src1_sel:DWORD
	v_add3_u32 v120, v106, v109, s43
	v_add3_u32 v121, v112, v108, s43
	v_and_b32_sdwa v108, v113, v185 dst_sel:DWORD dst_unused:UNUSED_PAD src0_sel:WORD_1 src1_sel:DWORD
	v_and_b32_sdwa v109, v107, v185 dst_sel:DWORD dst_unused:UNUSED_PAD src0_sel:WORD_1 src1_sel:DWORD
	v_add3_u32 v122, v113, v108, s43
	v_add3_u32 v123, v107, v109, s43
	v_mov_b32_e32 v108, v1
	v_mov_b32_e32 v109, v1
	v_cvt_pk_fp8_f32 v108, v100, v101
	v_cvt_pk_fp8_f32 v109, v106, v107
	v_and_b32_e32 v100, 0xffff0000, v122
	v_and_b32_e32 v106, 0xffff0000, v123
	v_cvt_pk_fp8_f32 v108, v104, v105 op_sel:[0,0,1]
	v_cvt_pk_fp8_f32 v109, v112, v113 op_sel:[0,0,1]
	v_or_b32_sdwa v101, v100, v121 dst_sel:DWORD dst_unused:UNUSED_PAD src0_sel:DWORD src1_sel:WORD_1
	v_or_b32_sdwa v100, v106, v120 dst_sel:DWORD dst_unused:UNUSED_PAD src0_sel:DWORD src1_sel:WORD_1
	global_store_dwordx2 v[102:103], v[126:127], off
	global_store_dwordx4 v[110:111], v[98:101], off offset:1024
	global_store_dwordx2 v[102:103], v[108:109], off offset:512
	v_lshl_add_u64 v[116:117], v[116:117], 0, s[54:55]
	s_waitcnt vmcnt(6)
	v_mov_b32_e32 v102, v54
	v_mov_b32_e32 v103, v55
	v_mov_b32_e32 v104, v56
	v_mov_b32_e32 v105, v57
	v_mov_b32_e32 v98, v50
	v_mov_b32_e32 v99, v51
	v_mov_b32_e32 v100, v52
	v_mov_b32_e32 v101, v53
	v_mov_b32_e32 v110, v38
	v_mov_b32_e32 v111, v39
	v_mov_b32_e32 v112, v40
	v_mov_b32_e32 v113, v41
	v_mov_b32_e32 v106, v34
	v_mov_b32_e32 v107, v35
	v_mov_b32_e32 v108, v36
	v_mov_b32_e32 v109, v37
	s_cbranch_scc0 .LBB0_758

; #define RP_UNPK(V_, H_) ((H_) ? (f32x4){bflo((V_)[2]), bfhi((V_)[2]), bflo((V_)[3]), bfhi((V_)[3])} : (f32x4){bflo((V_)[0]), bfhi((V_)[0]), bflo((V_)[1]), bfhi((V_)[1])})
; template <int MODE, bool FIRSTX>
; __device__ __forceinline__ void row_pass(Frame& F, int layer, bool final_out, int row0) {
;     ...
;         f32x4 v[4];
; #pragma unroll
;         for (int q = 0; q < 4; ++q) v[q] = FIRSTX ? xf[q] : RP_UNPK(xb[q >> 1], q & 1);
;         if (MODE != 0) {
; #pragma unroll
;             for (int q = 0; q < 4; ++q) { f32x4 y = (f32x4){0.f, 0.f, 0.f, 0.f};
; #pragma unroll
;                 for (int k = 0; k < NY; ++k) { if (MODE == 2) { const unsigned w8 = yb[k][q >> 1][q & 1]; const f32x2 lo = __builtin_amdgcn_cvt_pk_f32_fp8((int)w8, false), hi = __builtin_amdgcn_cvt_pk_f32_fp8((int)w8, true); y += (f32x4){lo.x, lo.y, hi.x, hi.y}; }
;                                                 else y += RP_UNPK(yb[k][q >> 1], q & 1); }
;                 if (MODE == 2) y = y * (1.0f / YK8_SCALE);
;                 v[q] = v[q] * DN_ALPHA + gt[q] * y; }
;             float s = 0.f;
; #pragma unroll
;             for (int q = 0; q < 4; ++q) s += (v[q][0] + v[q][1]) + (v[q][2] + v[q][3]);
;             const float mean = wave_sum(s) * (1.0f / DM); float qq = 0.f;
; #pragma unroll
;             for (int q = 0; q < 4; ++q) { v[q] = v[q] - mean; qq += (v[q][0] * v[q][0] + v[q][1] * v[q][1]) + (v[q][2] * v[q][2] + v[q][3] * v[q][3]); }
;             const float rstd = 1.0f / sqrtf(wave_sum(qq) * (1.0f / DM) + LN_EPS);
.Lrp1f_common:
	v_lshlrev_b32_e32 v138, 16, v122
	v_and_b32_e32 v139, 0xffff0000, v122
	v_lshlrev_b32_e32 v122, 16, v123
	v_and_b32_e32 v123, 0xffff0000, v123
	v_pk_add_f32 v[122:123], v[122:123], 0 op_sel_hi:[1,0]
	v_pk_add_f32 v[138:139], v[138:139], 0 op_sel_hi:[1,0]
	v_pk_mul_f32 v[122:123], v[122:123], v[40:41]
	v_pk_mul_f32 v[138:139], v[138:139], v[38:39]
	v_pk_fma_f32 v[122:123], v[128:129], s[62:63], v[122:123] op_sel_hi:[1,0,1]
	v_lshlrev_b32_e32 v128, 16, v124
	v_and_b32_e32 v129, 0xffff0000, v124
	v_lshlrev_b32_e32 v124, 16, v125
	v_and_b32_e32 v125, 0xffff0000, v125
	v_pk_add_f32 v[124:125], v[124:125], 0 op_sel_hi:[1,0]
	v_pk_add_f32 v[128:129], v[128:129], 0 op_sel_hi:[1,0]
	v_pk_mul_f32 v[124:125], v[124:125], v[36:37]
	v_pk_fma_f32 v[126:127], v[126:127], s[62:63], v[138:139] op_sel_hi:[1,0,1]
	v_pk_fma_f32 v[120:121], v[120:121], s[62:63], v[124:125] op_sel_hi:[1,0,1]
	v_lshlrev_b32_e32 v124, 16, v114
	v_and_b32_e32 v125, 0xffff0000, v114
	v_lshlrev_b32_e32 v114, 16, v115
	v_and_b32_e32 v115, 0xffff0000, v115
	v_pk_add_f32 v[114:115], v[114:115], 0 op_sel_hi:[1,0]
	v_pk_mul_f32 v[128:129], v[128:129], v[34:35]
	v_pk_mul_f32 v[114:115], v[114:115], v[64:65]
	v_pk_fma_f32 v[118:119], v[118:119], s[62:63], v[128:129] op_sel_hi:[1,0,1]
	v_pk_fma_f32 v[112:113], v[112:113], s[62:63], v[114:115] op_sel_hi:[1,0,1]
	v_lshlrev_b32_e32 v114, 16, v116
	v_and_b32_e32 v115, 0xffff0000, v116
	v_lshlrev_b32_e32 v116, 16, v117
	v_and_b32_e32 v117, 0xffff0000, v117
	v_pk_add_f32 v[114:115], v[114:115], 0 op_sel_hi:[1,0]
	v_pk_add_f32 v[116:117], v[116:117], 0 op_sel_hi:[1,0]
	v_pk_mul_f32 v[114:115], v[114:115], v[54:55]
	v_pk_add_f32 v[124:125], v[124:125], 0 op_sel_hi:[1,0]
	v_pk_mul_f32 v[116:117], v[116:117], v[56:57]
	v_pk_fma_f32 v[106:107], v[106:107], s[62:63], v[114:115] op_sel_hi:[1,0,1]
	v_add_f32_e32 v114, v126, v127
	v_add_f32_e32 v115, v122, v123
	v_pk_mul_f32 v[124:125], v[124:125], v[62:63]
	v_pk_fma_f32 v[108:109], v[108:109], s[62:63], v[116:117] op_sel_hi:[1,0,1]
	v_add_f32_e32 v114, v114, v115
	v_add_f32_e32 v115, v118, v119
	v_add_f32_e32 v116, v120, v121
	v_pk_fma_f32 v[110:111], v[110:111], s[62:63], v[124:125] op_sel_hi:[1,0,1]
	v_add_f32_e32 v114, 0, v114
	v_add_f32_e32 v115, v115, v116
	v_add_f32_e32 v114, v115, v114
	v_add_f32_e32 v115, v110, v111
	v_add_f32_e32 v116, v112, v113
	v_add_f32_e32 v115, v115, v116
	v_add_f32_e32 v114, v115, v114
	v_add_f32_e32 v115, v106, v107
	v_add_f32_e32 v116, v108, v109
	v_add_f32_e32 v115, v115, v116
	v_add_f32_e32 v114, v115, v114
	s_nop 1
	v_add_f32_dpp v114, v114, v114 quad_perm:[1,0,3,2] row_mask:0xf bank_mask:0xf
	s_add_u32 s76, s76, 1
	s_addc_u32 s77, s77, 0
	s_nop 1
	v_add_f32_dpp v114, v114, v114 quad_perm:[2,3,0,1] row_mask:0xf bank_mask:0xf
	s_nop 1
	v_add_f32_dpp v114, v114, v114 row_half_mirror row_mask:0xf bank_mask:0xf
	s_nop 1
	v_add_f32_dpp v114, v114, v114 row_mirror row_mask:0xf bank_mask:0xf
	s_waitcnt lgkmcnt(0)
	v_mov_b32_e32 v115, v114
	s_nop 1
	v_permlane16_swap_b32_e32 v114, v115
	v_add_f32_e32 v114, v114, v115
	v_mov_b32_e32 v115, v114
	s_nop 1
	v_permlane32_swap_b32_e32 v114, v115
	v_add_f32_e32 v114, v114, v115
	v_fmac_f32_e32 v123, 0xba800000, v114
	v_fmac_f32_e32 v127, 0xba800000, v114
	v_fmamk_f32 v122, v114, 0xba800000, v122
	v_fmamk_f32 v126, v114, 0xba800000, v126
	v_mul_f32_e32 v115, v127, v127
	v_mul_f32_e32 v116, v123, v123
	v_fmac_f32_e32 v115, v126, v126
	v_fmac_f32_e32 v116, v122, v122
	v_fmac_f32_e32 v121, 0xba800000, v114
	v_fmac_f32_e32 v119, 0xba800000, v114
	v_add_f32_e32 v115, v115, v116
	v_fmamk_f32 v120, v114, 0xba800000, v120
	v_fmamk_f32 v118, v114, 0xba800000, v118
	v_mul_f32_e32 v116, v119, v119
	v_mul_f32_e32 v117, v121, v121
	v_fmac_f32_e32 v116, v118, v118
	v_fmac_f32_e32 v117, v120, v120
	v_add_f32_e32 v116, v116, v117
	v_fmac_f32_e32 v113, 0xba800000, v114
	v_fmac_f32_e32 v111, 0xba800000, v114
	v_add_f32_e32 v115, v115, v116
	v_fmamk_f32 v112, v114, 0xba800000, v112
	v_fmamk_f32 v110, v114, 0xba800000, v110
	v_mul_f32_e32 v116, v111, v111
	v_mul_f32_e32 v117, v113, v113
	v_fmac_f32_e32 v116, v110, v110
	v_fmac_f32_e32 v117, v112, v112
	v_add_f32_e32 v116, v116, v117
	v_fmac_f32_e32 v109, 0xba800000, v114
	v_fmac_f32_e32 v107, 0xba800000, v114
	v_add_f32_e32 v115, v116, v115
	v_fmamk_f32 v108, v114, 0xba800000, v108
	v_fmamk_f32 v106, v114, 0xba800000, v106
	v_mul_f32_e32 v114, v107, v107
	v_mul_f32_e32 v116, v109, v109
	v_fmac_f32_e32 v114, v106, v106
	v_fmac_f32_e32 v116, v108, v108
	v_add_f32_e32 v114, v114, v116
	v_add_f32_e32 v114, v114, v115
	s_nop 1
	v_add_f32_dpp v114, v114, v114 quad_perm:[1,0,3,2] row_mask:0xf bank_mask:0xf
	s_nop 1
	v_add_f32_dpp v114, v114, v114 quad_perm:[2,3,0,1] row_mask:0xf bank_mask:0xf
	s_nop 1
	v_add_f32_dpp v114, v114, v114 row_half_mirror row_mask:0xf bank_mask:0xf
	s_nop 1
	v_add_f32_dpp v114, v114, v114 row_mirror row_mask:0xf bank_mask:0xf
	s_waitcnt lgkmcnt(0)
; __device__ __forceinline__ unsigned pk2(float lo, float hi) { return f2bf(lo) | (f2bf(hi) << 16); }
; __device__ __forceinline__ unsigned cvt_fp8x4(float a, float b, float c, float d) { int w = __builtin_amdgcn_cvt_pk_fp8_f32(a, b, 0, false); w = __builtin_amdgcn_cvt_pk_fp8_f32(c, d, w, true); return (unsigned)w; }
; template <int MODE, bool FIRSTX>
; __device__ __forceinline__ void row_pass(Frame& F, int layer, bool final_out, int row0) {
;     ...
;             const float rstd = 1.0f / sqrtf(wave_sum(qq) * (1.0f / DM) + LN_EPS);
; #pragma unroll
;             for (int q = 0; q < 4; ++q) v[q] = v[q] * rstd * lg[q] + lb[q];
;             if (final_out) { if (row >= NCTX) {
; #pragma unroll
;                 for (int q = 0; q < 4; ++q) *(f32x4*)(F.out + (size_t)(row - NCTX) * DM + RP_COL(q)) = v[q]; } }
;             else {
; #pragma unroll
;                 for (int j = 0; j < 2; ++j) { u32x4 w; w.x = pk2(v[2 * j][0], v[2 * j][1]); w.y = pk2(v[2 * j][2], v[2 * j][3]); w.z = pk2(v[2 * j + 1][0], v[2 * j + 1][1]); w.w = pk2(v[2 * j + 1][2], v[2 * j + 1][3]);
;                     *(u32x4*)(X + (size_t)row * DM + lc + 512 * j) = w; } }
;         }
;         if (!final_out) {
; #pragma unroll
;             for (int j = 0; j < 2; ++j) { const f32x4 h0 = v[2 * j] * (sc[2 * j] + 1.0f) + sh[2 * j], h1 = v[2 * j + 1] * (sc[2 * j + 1] + 1.0f) + sh[2 * j + 1];
;                 if (MODE == 1 || (nlayer % 3) == 2) { u32x4 w; w.x = pk2(h0[0], h0[1]); w.y = pk2(h0[2], h0[3]); w.z = pk2(h1[0], h1[1]); w.w = pk2(h1[2], h1[3]);
;                     *(u32x4*)(H + (size_t)row * DM + lc + 512 * j) = w; }
;                 if (MODE == 1 || (nlayer % 3) != 2) {                                u32x2 w8; w8.x = cvt_fp8x4(h0[0], h0[1], h0[2], h0[3]); w8.y = cvt_fp8x4(h1[0], h1[1], h1[2], h1[3]); *(u32x2*)(F.ws + WS_H8 + (size_t)row * DM + lc + 512 * j) = w8; } }
	v_mov_b32_e32 v115, v114
	s_nop 1
	v_permlane16_swap_b32_e32 v114, v115
	v_add_f32_e32 v114, v114, v115
	v_mov_b32_e32 v115, v114
	s_nop 1
	v_permlane32_swap_b32_e32 v114, v115
	v_add_f32_e32 v114, v114, v115
	v_fmamk_f32 v114, v114, 0x3a800000, v188
	v_mul_f32_e32 v115, 0x4f800000, v114
	v_cmp_gt_f32_e32 vcc, s31, v114
	s_nop 1
	v_cndmask_b32_e32 v114, v114, v115, vcc
	v_sqrt_f32_e32 v115, v114
	s_nop 0
	v_add_u32_e32 v116, -1, v115
	v_fma_f32 v117, -v116, v115, v114
	v_cmp_ge_f32_e64 s[2:3], 0, v117
	v_add_u32_e32 v117, 1, v115
	s_nop 0
	v_cndmask_b32_e64 v116, v115, v116, s[2:3]
	v_fma_f32 v115, -v117, v115, v114
	v_cmp_lt_f32_e64 s[2:3], 0, v115
	s_nop 1
	v_cndmask_b32_e64 v115, v116, v117, s[2:3]
	v_mul_f32_e32 v116, 0x37800000, v115
	v_cndmask_b32_e32 v115, v115, v116, vcc
	v_cmp_class_f32_e32 vcc, v114, v189
	s_nop 1
	v_cndmask_b32_e32 v114, v115, v114, vcc
	v_div_scale_f32 v115, s[0:1], v114, v114, 1.0
	v_rcp_f32_e32 v116, v115
	s_add_i32 s0, s4, s76
	s_add_u32 s60, s60, 0x1000
	s_addc_u32 s61, s61, 0
	v_fma_f32 v117, -v115, v116, 1.0
	v_fmac_f32_e32 v116, v117, v116
	v_div_scale_f32 v117, vcc, 1.0, v114, 1.0
	v_mul_f32_e32 v124, v117, v116
	v_fma_f32 v125, -v115, v124, v117
	v_fmac_f32_e32 v124, v125, v116
	v_fma_f32 v115, -v115, v124, v117
	v_div_fmas_f32 v115, v115, v116, v124
	v_div_fixup_f32 v114, v115, v114, 1.0
	v_pk_mul_f32 v[116:117], v[126:127], v[114:115] op_sel_hi:[1,0]
	v_pk_mul_f32 v[106:107], v[106:107], v[114:115] op_sel_hi:[1,0]
	v_pk_fma_f32 v[116:117], v[2:3], v[116:117], v[6:7]
	v_pk_mul_f32 v[122:123], v[122:123], v[114:115] op_sel_hi:[1,0]
	v_pk_mul_f32 v[118:119], v[118:119], v[114:115] op_sel_hi:[1,0]
	v_pk_mul_f32 v[120:121], v[120:121], v[114:115] op_sel_hi:[1,0]
	v_pk_mul_f32 v[110:111], v[110:111], v[114:115] op_sel_hi:[1,0]
	v_pk_mul_f32 v[112:113], v[112:113], v[114:115] op_sel_hi:[1,0]
	v_pk_mul_f32 v[108:109], v[108:109], v[114:115] op_sel_hi:[1,0]
	v_pk_fma_f32 v[114:115], v[26:27], v[106:107], v[30:31]
	v_bfe_u32 v106, v116, 16, 1
	v_add3_u32 v106, v116, v106, s43
	v_bfe_u32 v107, v117, 16, 1
	v_pk_fma_f32 v[122:123], v[4:5], v[122:123], v[8:9]
	v_lshrrev_b32_e32 v106, 16, v106
	v_add3_u32 v107, v117, v107, s43
	v_and_or_b32 v106, v107, s33, v106
	v_bfe_u32 v107, v122, 16, 1
	v_pk_fma_f32 v[124:125], v[28:29], v[108:109], v[32:33]
	v_add3_u32 v107, v122, v107, s43
	v_bfe_u32 v108, v123, 16, 1
	v_pk_fma_f32 v[118:119], v[10:11], v[118:119], v[14:15]
	v_lshrrev_b32_e32 v107, 16, v107
	v_add3_u32 v108, v123, v108, s43
	v_and_or_b32 v107, v108, s33, v107
	v_bfe_u32 v108, v118, 16, 1
	v_add3_u32 v108, v118, v108, s43
	v_bfe_u32 v109, v119, 16, 1
	v_pk_fma_f32 v[120:121], v[12:13], v[120:121], v[16:17]
	v_lshrrev_b32_e32 v108, 16, v108
	v_add3_u32 v109, v119, v109, s43
	v_and_or_b32 v108, v109, s33, v108
	v_bfe_u32 v109, v120, 16, 1
	v_add3_u32 v109, v120, v109, s43
	v_bfe_u32 v128, v121, 16, 1
	v_lshl_add_u64 v[126:127], s[74:75], 0, v[132:133]
	v_lshrrev_b32_e32 v109, 16, v109
	v_add3_u32 v128, v121, v128, s43
	v_and_or_b32 v109, v128, s33, v109
	v_add_co_u32_e32 v128, vcc, s39, v126
	v_pk_fma_f32 v[110:111], v[18:19], v[110:111], v[22:23]
	s_nop 0
	v_addc_co_u32_e32 v129, vcc, 0, v127, vcc
	global_store_dwordx4 v[128:129], v[106:109], off
	v_pk_fma_f32 v[112:113], v[20:21], v[112:113], v[24:25]
	v_bfe_u32 v137, v125, 16, 1
	v_bfe_u32 v106, v110, 16, 1
	v_add3_u32 v106, v110, v106, s43
	v_bfe_u32 v107, v111, 16, 1
	v_lshrrev_b32_e32 v106, 16, v106
	v_add3_u32 v107, v111, v107, s43
	v_and_or_b32 v106, v107, s33, v106
	v_bfe_u32 v107, v112, 16, 1
	v_add3_u32 v107, v112, v107, s43
	v_bfe_u32 v108, v113, 16, 1
	v_lshrrev_b32_e32 v107, 16, v107
	v_add3_u32 v108, v113, v108, s43
	v_and_or_b32 v107, v108, s33, v107
	v_bfe_u32 v108, v114, 16, 1
	v_add3_u32 v108, v114, v108, s43
	v_bfe_u32 v109, v115, 16, 1
	v_lshrrev_b32_e32 v108, 16, v108
	v_add3_u32 v109, v115, v109, s43
	v_and_or_b32 v108, v109, s33, v108
	v_bfe_u32 v109, v124, 16, 1
	v_add3_u32 v109, v124, v109, s43
	v_lshrrev_b32_e32 v109, 16, v109
	v_add3_u32 v137, v125, v137, s43
	v_and_or_b32 v109, v137, s33, v109
	global_store_dwordx4 v[128:129], v[106:109], off offset:1024
	v_lshl_add_u64 v[132:133], v[132:133], 0, s[50:51]
	s_cmp_ge_i32 s0, s11
	v_pk_add_f32 v[106:107], v[60:61], 1.0 op_sel_hi:[1,0]
	v_pk_add_f32 v[108:109], v[58:59], 1.0 op_sel_hi:[1,0]
	v_pk_fma_f32 v[122:123], v[106:107], v[122:123], v[48:49]
	v_pk_fma_f32 v[116:117], v[108:109], v[116:117], v[46:47]
	v_pk_add_f32 v[106:107], v[52:53], 1.0 op_sel_hi:[1,0]
	v_pk_add_f32 v[108:109], v[50:51], 1.0 op_sel_hi:[1,0]
	v_pk_fma_f32 v[120:121], v[106:107], v[120:121], v[44:45]
	v_and_b32_sdwa v107, v116, v185 dst_sel:DWORD dst_unused:UNUSED_PAD src0_sel:WORD_1 src1_sel:DWORD
	v_pk_fma_f32 v[118:119], v[108:109], v[118:119], v[42:43]
	v_add3_u32 v108, v116, v107, s43
	v_and_b32_sdwa v107, v123, v185 dst_sel:DWORD dst_unused:UNUSED_PAD src0_sel:WORD_1 src1_sel:DWORD
; __device__ __forceinline__ unsigned pk2(float lo, float hi) { return f2bf(lo) | (f2bf(hi) << 16); }
; __device__ __forceinline__ unsigned cvt_fp8x4(float a, float b, float c, float d) { int w = __builtin_amdgcn_cvt_pk_fp8_f32(a, b, 0, false); w = __builtin_amdgcn_cvt_pk_fp8_f32(c, d, w, true); return (unsigned)w; }
; template <int MODE, bool FIRSTX>
; __device__ __forceinline__ void row_pass(Frame& F, int layer, bool final_out, int row0) {
;     ...
;         if (!final_out) {
; #pragma unroll
;             for (int j = 0; j < 2; ++j) { const f32x4 h0 = v[2 * j] * (sc[2 * j] + 1.0f) + sh[2 * j], h1 = v[2 * j + 1] * (sc[2 * j + 1] + 1.0f) + sh[2 * j + 1];
;                 if (MODE == 1 || (nlayer % 3) == 2) { u32x4 w; w.x = pk2(h0[0], h0[1]); w.y = pk2(h0[2], h0[3]); w.z = pk2(h1[0], h1[1]); w.w = pk2(h1[2], h1[3]);
;                     *(u32x4*)(H + (size_t)row * DM + lc + 512 * j) = w; }
;                 if (MODE == 1 || (nlayer % 3) != 2) {                                u32x2 w8; w8.x = cvt_fp8x4(h0[0], h0[1], h0[2], h0[3]); w8.y = cvt_fp8x4(h1[0], h1[1], h1[2], h1[3]); *(u32x2*)(F.ws + WS_H8 + (size_t)row * DM + lc + 512 * j) = w8; } }
;         }
; #pragma unroll
;         for (int q = 0; q < 4; ++q) xf[q] = xfn[q];
; #pragma unroll
;         for (int j = 0; j < 2; ++j) { xb[j] = xbn[j];
; #pragma unroll
;             for (int k = 0; k < (NY ? NY : 1); ++k) yb[k][j] = ybn[k][j]; }
	v_and_b32_sdwa v109, v117, v185 dst_sel:DWORD dst_unused:UNUSED_PAD src0_sel:WORD_1 src1_sel:DWORD
	v_and_b32_sdwa v106, v122, v185 dst_sel:DWORD dst_unused:UNUSED_PAD src0_sel:WORD_1 src1_sel:DWORD
	v_add3_u32 v107, v123, v107, s43
	v_add3_u32 v109, v117, v109, s43
	v_add3_u32 v106, v122, v106, s43
	v_and_b32_e32 v107, 0xffff0000, v107
	v_and_b32_e32 v109, 0xffff0000, v109
	v_or_b32_sdwa v107, v107, v106 dst_sel:DWORD dst_unused:UNUSED_PAD src0_sel:DWORD src1_sel:WORD_1
	v_or_b32_sdwa v106, v109, v108 dst_sel:DWORD dst_unused:UNUSED_PAD src0_sel:DWORD src1_sel:WORD_1
	v_and_b32_sdwa v109, v118, v185 dst_sel:DWORD dst_unused:UNUSED_PAD src0_sel:WORD_1 src1_sel:DWORD
	v_add3_u32 v128, v118, v109, s43
	v_and_b32_sdwa v109, v121, v185 dst_sel:DWORD dst_unused:UNUSED_PAD src0_sel:WORD_1 src1_sel:DWORD
	v_and_b32_sdwa v129, v119, v185 dst_sel:DWORD dst_unused:UNUSED_PAD src0_sel:WORD_1 src1_sel:DWORD
	v_and_b32_sdwa v108, v120, v185 dst_sel:DWORD dst_unused:UNUSED_PAD src0_sel:WORD_1 src1_sel:DWORD
	v_add3_u32 v109, v121, v109, s43
	v_add3_u32 v129, v119, v129, s43
	v_add3_u32 v108, v120, v108, s43
	v_and_b32_e32 v109, 0xffff0000, v109
	v_and_b32_e32 v129, 0xffff0000, v129
	v_or_b32_sdwa v109, v109, v108 dst_sel:DWORD dst_unused:UNUSED_PAD src0_sel:DWORD src1_sel:WORD_1
	v_or_b32_sdwa v108, v129, v128 dst_sel:DWORD dst_unused:UNUSED_PAD src0_sel:DWORD src1_sel:WORD_1
	v_mov_b32_e32 v128, v1
	v_cvt_pk_fp8_f32 v128, v116, v117
	v_add_co_u32_e32 v116, vcc, s28, v126
	v_mov_b32_e32 v129, v1
	s_nop 0
	v_addc_co_u32_e32 v117, vcc, 0, v127, vcc
	v_cvt_pk_fp8_f32 v129, v118, v119
	global_store_dwordx4 v[116:117], v[106:109], off
	v_cvt_pk_fp8_f32 v128, v122, v123 op_sel:[0,0,1]
	v_cvt_pk_fp8_f32 v129, v120, v121 op_sel:[0,0,1]
	v_lshl_add_u64 v[106:107], s[74:75], 0, v[134:135]
	v_add_co_u32_e32 v118, vcc, s38, v106
	v_pk_add_f32 v[108:109], v[78:79], 1.0 op_sel_hi:[1,0]
	s_nop 0
	v_addc_co_u32_e32 v119, vcc, 0, v107, vcc
	v_pk_add_f32 v[106:107], v[80:81], 1.0 op_sel_hi:[1,0]
	v_pk_fma_f32 v[108:109], v[108:109], v[110:111], v[70:71]
	v_pk_fma_f32 v[112:113], v[106:107], v[112:113], v[72:73]
	v_pk_add_f32 v[106:107], v[76:77], 1.0 op_sel_hi:[1,0]
	v_pk_add_f32 v[110:111], v[74:75], 1.0 op_sel_hi:[1,0]
	v_pk_fma_f32 v[120:121], v[106:107], v[124:125], v[68:69]
	v_and_b32_sdwa v107, v108, v185 dst_sel:DWORD dst_unused:UNUSED_PAD src0_sel:WORD_1 src1_sel:DWORD
	v_pk_fma_f32 v[110:111], v[110:111], v[114:115], v[66:67]
	v_add3_u32 v114, v108, v107, s43
	v_and_b32_sdwa v107, v113, v185 dst_sel:DWORD dst_unused:UNUSED_PAD src0_sel:WORD_1 src1_sel:DWORD
	v_and_b32_sdwa v115, v109, v185 dst_sel:DWORD dst_unused:UNUSED_PAD src0_sel:WORD_1 src1_sel:DWORD
	v_and_b32_sdwa v106, v112, v185 dst_sel:DWORD dst_unused:UNUSED_PAD src0_sel:WORD_1 src1_sel:DWORD
	v_add3_u32 v107, v113, v107, s43
	v_add3_u32 v115, v109, v115, s43
	v_add3_u32 v106, v112, v106, s43
	v_and_b32_e32 v107, 0xffff0000, v107
	v_and_b32_e32 v115, 0xffff0000, v115
	v_or_b32_sdwa v107, v107, v106 dst_sel:DWORD dst_unused:UNUSED_PAD src0_sel:DWORD src1_sel:WORD_1
	v_or_b32_sdwa v106, v115, v114 dst_sel:DWORD dst_unused:UNUSED_PAD src0_sel:DWORD src1_sel:WORD_1
	v_and_b32_sdwa v114, v120, v185 dst_sel:DWORD dst_unused:UNUSED_PAD src0_sel:WORD_1 src1_sel:DWORD
	v_and_b32_sdwa v115, v110, v185 dst_sel:DWORD dst_unused:UNUSED_PAD src0_sel:WORD_1 src1_sel:DWORD
	v_add3_u32 v122, v110, v115, s43
	v_add3_u32 v123, v120, v114, s43
	v_and_b32_sdwa v114, v121, v185 dst_sel:DWORD dst_unused:UNUSED_PAD src0_sel:WORD_1 src1_sel:DWORD
	v_and_b32_sdwa v115, v111, v185 dst_sel:DWORD dst_unused:UNUSED_PAD src0_sel:WORD_1 src1_sel:DWORD
	v_add3_u32 v124, v121, v114, s43
	v_add3_u32 v125, v111, v115, s43
	v_mov_b32_e32 v114, v1
	v_mov_b32_e32 v115, v1
	v_cvt_pk_fp8_f32 v114, v108, v109
	v_cvt_pk_fp8_f32 v115, v110, v111
	v_and_b32_e32 v108, 0xffff0000, v124
	v_and_b32_e32 v110, 0xffff0000, v125
	v_cvt_pk_fp8_f32 v114, v112, v113 op_sel:[0,0,1]
	v_cvt_pk_fp8_f32 v115, v120, v121 op_sel:[0,0,1]
	v_or_b32_sdwa v109, v108, v123 dst_sel:DWORD dst_unused:UNUSED_PAD src0_sel:DWORD src1_sel:WORD_1
	v_or_b32_sdwa v108, v110, v122 dst_sel:DWORD dst_unused:UNUSED_PAD src0_sel:DWORD src1_sel:WORD_1
	global_store_dwordx2 v[118:119], v[128:129], off
	global_store_dwordx4 v[116:117], v[106:109], off offset:1024
	global_store_dwordx2 v[118:119], v[114:115], off offset:512
	s_waitcnt vmcnt(6)
	v_mov_b64_e32 v[112:113], v[96:97]
	v_mov_b64_e32 v[108:109], v[92:93]
	v_mov_b64_e32 v[120:121], v[84:85]
	v_mov_b64_e32 v[128:129], v[88:89]
	v_lshl_add_u64 v[134:135], v[134:135], 0, s[54:55]
	v_mov_b64_e32 v[106:107], v[90:91]
	v_mov_b64_e32 v[110:111], v[94:95]
	v_mov_b64_e32 v[118:119], v[82:83]
	v_mov_b64_e32 v[126:127], v[86:87]
	v_mov_b32_e32 v122, v98
	v_mov_b32_e32 v123, v99
	v_mov_b32_e32 v124, v100
	v_mov_b32_e32 v125, v101
	v_mov_b32_e32 v114, v102
	v_mov_b32_e32 v115, v103
	v_mov_b32_e32 v116, v104
	v_mov_b32_e32 v117, v105
	s_cbranch_scc1 .LBB0_777

; #define RP_UNPK(V_, H_) ((H_) ? (f32x4){bflo((V_)[2]), bfhi((V_)[2]), bflo((V_)[3]), bfhi((V_)[3])} : (f32x4){bflo((V_)[0]), bfhi((V_)[0]), bflo((V_)[1]), bfhi((V_)[1])})
; template <int MODE, bool FIRSTX>
; __device__ __forceinline__ void row_pass(Frame& F, int layer, bool final_out, int row0) {
;     ...
;         if (MODE != 0) {
; #pragma unroll
;             for (int q = 0; q < 4; ++q) { f32x4 y = (f32x4){0.f, 0.f, 0.f, 0.f};
; #pragma unroll
;                 for (int k = 0; k < NY; ++k) { if (MODE == 2) { const unsigned w8 = yb[k][q >> 1][q & 1]; const f32x2 lo = __builtin_amdgcn_cvt_pk_f32_fp8((int)w8, false), hi = __builtin_amdgcn_cvt_pk_f32_fp8((int)w8, true); y += (f32x4){lo.x, lo.y, hi.x, hi.y}; }
;                                                 else y += RP_UNPK(yb[k][q >> 1], q & 1); }
;                 if (MODE == 2) y = y * (1.0f / YK8_SCALE);
;                 v[q] = v[q] * DN_ALPHA + gt[q] * y; }
;             float s = 0.f;
; #pragma unroll
;             for (int q = 0; q < 4; ++q) s += (v[q][0] + v[q][1]) + (v[q][2] + v[q][3]);
;             const float mean = wave_sum(s) * (1.0f / DM); float qq = 0.f;
.LBB0_1210:
	v_lshlrev_b32_e32 v154, 16, v96
	v_and_b32_e32 v155, 0xffff0000, v96
	v_lshlrev_b32_e32 v156, 16, v97
	v_and_b32_e32 v157, 0xffff0000, v97
	v_lshlrev_b32_e32 v158, 16, v90
	v_and_b32_e32 v159, 0xffff0000, v90
	v_lshlrev_b32_e32 v160, 16, v91
	v_and_b32_e32 v161, 0xffff0000, v91
	v_lshlrev_b32_e32 v96, 16, v92
	v_and_b32_e32 v97, 0xffff0000, v92
	v_lshlrev_b32_e32 v150, 16, v93
	v_and_b32_e32 v151, 0xffff0000, v93
	v_cvt_pk_f32_fp8_e32 v[90:91], v142
	v_cvt_pk_f32_fp8_sdwa v[92:93], v142 src0_sel:WORD_1
	v_cvt_pk_f32_fp8_e32 v[162:163], v140
	v_cvt_pk_f32_fp8_sdwa v[164:165], v140 src0_sel:WORD_1
	v_pk_add_f32 v[90:91], v[90:91], 0 op_sel_hi:[1,0]
	v_pk_add_f32 v[92:93], v[92:93], 0 op_sel_hi:[1,0]
	v_pk_add_f32 v[90:91], v[90:91], v[162:163]
	v_pk_add_f32 v[92:93], v[92:93], v[164:165]
	v_cvt_pk_f32_fp8_e32 v[162:163], v144
	v_cvt_pk_f32_fp8_sdwa v[164:165], v144 src0_sel:WORD_1
	v_lshlrev_b32_e32 v152, 16, v94
	v_and_b32_e32 v153, 0xffff0000, v94
	v_pk_add_f32 v[90:91], v[90:91], v[162:163]
	v_pk_add_f32 v[92:93], v[92:93], v[164:165]
	v_cvt_pk_f32_fp8_e32 v[162:163], v148
	v_cvt_pk_f32_fp8_sdwa v[164:165], v148 src0_sel:WORD_1
	v_lshlrev_b32_e32 v94, 16, v95
	v_and_b32_e32 v95, 0xffff0000, v95
	v_pk_add_f32 v[90:91], v[90:91], v[162:163]
	v_pk_add_f32 v[92:93], v[92:93], v[164:165]
	v_pk_mul_f32 v[90:91], v[90:91], s[70:71] op_sel_hi:[1,0]
	v_pk_mul_f32 v[92:93], v[92:93], s[70:71] op_sel_hi:[1,0]
	v_pk_mul_f32 v[162:163], v[70:71], v[90:91]
	v_pk_mul_f32 v[90:91], v[72:73], v[92:93]
	v_pk_fma_f32 v[92:93], v[152:153], s[62:63], v[162:163] op_sel_hi:[1,0,1]
	v_pk_fma_f32 v[90:91], v[94:95], s[62:63], v[90:91] op_sel_hi:[1,0,1]
	v_cvt_pk_f32_fp8_e32 v[94:95], v143
	v_cvt_pk_f32_fp8_sdwa v[142:143], v143 src0_sel:WORD_1
	v_cvt_pk_f32_fp8_e32 v[152:153], v141
	v_cvt_pk_f32_fp8_sdwa v[140:141], v141 src0_sel:WORD_1
	v_pk_add_f32 v[94:95], v[94:95], 0 op_sel_hi:[1,0]
	v_pk_add_f32 v[142:143], v[142:143], 0 op_sel_hi:[1,0]
	v_pk_add_f32 v[94:95], v[94:95], v[152:153]
	v_pk_add_f32 v[140:141], v[142:143], v[140:141]
	v_cvt_pk_f32_fp8_e32 v[142:143], v145
	v_cvt_pk_f32_fp8_sdwa v[144:145], v145 src0_sel:WORD_1
	v_cvt_pk_f32_fp8_sdwa v[152:153], v98 src0_sel:WORD_1
	v_add_f32_e32 v0, v92, v93
	v_pk_add_f32 v[94:95], v[94:95], v[142:143]
	v_cvt_pk_f32_fp8_e32 v[142:143], v149
	v_pk_add_f32 v[140:141], v[140:141], v[144:145]
	v_cvt_pk_f32_fp8_sdwa v[144:145], v149 src0_sel:WORD_1
	v_cvt_pk_f32_fp8_e32 v[148:149], v98
	v_pk_add_f32 v[94:95], v[94:95], v[142:143]
	v_pk_add_f32 v[140:141], v[140:141], v[144:145]
	v_pk_mul_f32 v[94:95], v[94:95], s[70:71] op_sel_hi:[1,0]
	v_pk_mul_f32 v[140:141], v[140:141], s[70:71] op_sel_hi:[1,0]
	v_pk_mul_f32 v[142:143], v[74:75], v[94:95]
	v_pk_mul_f32 v[94:95], v[76:77], v[140:141]
	v_pk_fma_f32 v[140:141], v[154:155], s[62:63], v[142:143] op_sel_hi:[1,0,1]
	v_cvt_pk_f32_fp8_e32 v[142:143], v100
	v_cvt_pk_f32_fp8_sdwa v[144:145], v100 src0_sel:WORD_1
	v_pk_fma_f32 v[94:95], v[156:157], s[62:63], v[94:95] op_sel_hi:[1,0,1]
	v_pk_add_f32 v[142:143], v[142:143], 0 op_sel_hi:[1,0]
	v_pk_add_f32 v[144:145], v[144:145], 0 op_sel_hi:[1,0]
	v_pk_add_f32 v[142:143], v[142:143], v[148:149]
	v_cvt_pk_f32_fp8_e32 v[148:149], v102
	v_pk_add_f32 v[144:145], v[144:145], v[152:153]
	v_cvt_pk_f32_fp8_sdwa v[152:153], v102 src0_sel:WORD_1
	v_pk_add_f32 v[142:143], v[142:143], v[148:149]
	v_cvt_pk_f32_fp8_e32 v[148:149], v104
	v_pk_add_f32 v[144:145], v[144:145], v[152:153]
	v_cvt_pk_f32_fp8_sdwa v[152:153], v104 src0_sel:WORD_1
	v_pk_add_f32 v[142:143], v[142:143], v[148:149]
	v_cvt_pk_f32_fp8_e32 v[148:149], v101
	v_cvt_pk_f32_fp8_sdwa v[100:101], v101 src0_sel:WORD_1
	v_pk_add_f32 v[144:145], v[144:145], v[152:153]
	v_cvt_pk_f32_fp8_e32 v[152:153], v99
	v_cvt_pk_f32_fp8_sdwa v[98:99], v99 src0_sel:WORD_1
	v_pk_add_f32 v[100:101], v[100:101], 0 op_sel_hi:[1,0]
	v_pk_add_f32 v[148:149], v[148:149], 0 op_sel_hi:[1,0]
	v_pk_mul_f32 v[144:145], v[144:145], s[70:71] op_sel_hi:[1,0]
	v_pk_add_f32 v[98:99], v[100:101], v[98:99]
	v_cvt_pk_f32_fp8_e32 v[100:101], v103
	v_cvt_pk_f32_fp8_sdwa v[102:103], v103 src0_sel:WORD_1
	v_pk_add_f32 v[148:149], v[148:149], v[152:153]
	v_pk_mul_f32 v[142:143], v[142:143], s[70:71] op_sel_hi:[1,0]
	v_pk_add_f32 v[100:101], v[148:149], v[100:101]
	v_pk_add_f32 v[98:99], v[98:99], v[102:103]
	v_cvt_pk_f32_fp8_e32 v[102:103], v105
	v_cvt_pk_f32_fp8_sdwa v[104:105], v105 src0_sel:WORD_1
	v_pk_mul_f32 v[142:143], v[78:79], v[142:143]
	v_pk_mul_f32 v[144:145], v[80:81], v[144:145]
	v_pk_add_f32 v[100:101], v[100:101], v[102:103]
	v_pk_add_f32 v[98:99], v[98:99], v[104:105]
	v_pk_fma_f32 v[144:145], v[160:161], s[62:63], v[144:145] op_sel_hi:[1,0,1]
	v_pk_mul_f32 v[98:99], v[98:99], s[70:71] op_sel_hi:[1,0]
	v_pk_fma_f32 v[142:143], v[158:159], s[62:63], v[142:143] op_sel_hi:[1,0,1]
	v_pk_mul_f32 v[98:99], v[88:89], v[98:99]
	v_pk_mul_f32 v[100:101], v[100:101], s[70:71] op_sel_hi:[1,0]
	v_pk_fma_f32 v[148:149], v[150:151], s[62:63], v[98:99] op_sel_hi:[1,0,1]
	v_add_f32_e32 v98, v90, v91
	v_add_f32_e32 v0, v0, v98
	v_add_f32_e32 v98, v140, v141
	v_add_f32_e32 v99, v94, v95
	v_add_f32_e32 v0, 0, v0
	v_add_f32_e32 v98, v98, v99
	v_pk_mul_f32 v[100:101], v[86:87], v[100:101]
	v_add_f32_e32 v0, v0, v98
	v_add_f32_e32 v98, v142, v143
	v_add_f32_e32 v99, v144, v145
	v_pk_fma_f32 v[96:97], v[96:97], s[62:63], v[100:101] op_sel_hi:[1,0,1]
	v_add_f32_e32 v98, v98, v99
	v_add_f32_e32 v0, v0, v98
	v_add_f32_e32 v98, v96, v97
	v_add_f32_e32 v99, v148, v149
	v_add_f32_e32 v98, v98, v99
	v_add_f32_e32 v0, v0, v98
	s_nop 1
	v_add_f32_dpp v0, v0, v0 quad_perm:[1,0,3,2] row_mask:0xf bank_mask:0xf
	s_nop 1
	v_add_f32_dpp v0, v0, v0 quad_perm:[2,3,0,1] row_mask:0xf bank_mask:0xf
	s_nop 1
	v_add_f32_dpp v0, v0, v0 row_half_mirror row_mask:0xf bank_mask:0xf
	s_nop 1
	v_add_f32_dpp v0, v0, v0 row_mirror row_mask:0xf bank_mask:0xf
	s_waitcnt lgkmcnt(0)
; __device__ __forceinline__ unsigned pk2(float lo, float hi) { return f2bf(lo) | (f2bf(hi) << 16); }
; template <int MODE, bool FIRSTX>
; __device__ __forceinline__ void row_pass(Frame& F, int layer, bool final_out, int row0) {
;     ...
;             float s = 0.f;
; #pragma unroll
;             for (int q = 0; q < 4; ++q) s += (v[q][0] + v[q][1]) + (v[q][2] + v[q][3]);
;             const float mean = wave_sum(s) * (1.0f / DM); float qq = 0.f;
; #pragma unroll
;             for (int q = 0; q < 4; ++q) { v[q] = v[q] - mean; qq += (v[q][0] * v[q][0] + v[q][1] * v[q][1]) + (v[q][2] * v[q][2] + v[q][3] * v[q][3]); }
;             const float rstd = 1.0f / sqrtf(wave_sum(qq) * (1.0f / DM) + LN_EPS);
; #pragma unroll
;             for (int q = 0; q < 4; ++q) v[q] = v[q] * rstd * lg[q] + lb[q];
;             if (final_out) { if (row >= NCTX) {
; #pragma unroll
;                 for (int q = 0; q < 4; ++q) *(f32x4*)(F.out + (size_t)(row - NCTX) * DM + RP_COL(q)) = v[q]; } }
;             else {
; #pragma unroll
;                 for (int j = 0; j < 2; ++j) { u32x4 w; w.x = pk2(v[2 * j][0], v[2 * j][1]); w.y = pk2(v[2 * j][2], v[2 * j][3]); w.z = pk2(v[2 * j + 1][0], v[2 * j + 1][1]); w.w = pk2(v[2 * j + 1][2], v[2 * j + 1][3]);
;                     *(u32x4*)(X + (size_t)row * DM + lc + 512 * j) = w; } }
	v_mov_b32_e32 v98, v0
	s_nop 1
	v_permlane16_swap_b32_e32 v0, v98
	v_add_f32_e32 v0, v0, v98
	v_mov_b32_e32 v98, v0
	s_nop 1
	v_permlane32_swap_b32_e32 v0, v98
	v_add_f32_e32 v0, v0, v98
	v_fmac_f32_e32 v91, 0xba800000, v0
	v_fmac_f32_e32 v93, 0xba800000, v0
	v_fmamk_f32 v90, v0, 0xba800000, v90
	v_fmamk_f32 v92, v0, 0xba800000, v92
	v_mul_f32_e32 v98, v93, v93
	v_mul_f32_e32 v99, v91, v91
	v_fmac_f32_e32 v98, v92, v92
	v_fmac_f32_e32 v99, v90, v90
	v_fmac_f32_e32 v95, 0xba800000, v0
	v_fmac_f32_e32 v141, 0xba800000, v0
	v_add_f32_e32 v98, v98, v99
	v_fmamk_f32 v94, v0, 0xba800000, v94
	v_fmamk_f32 v140, v0, 0xba800000, v140
	v_mul_f32_e32 v99, v141, v141
	v_mul_f32_e32 v100, v95, v95
	v_fmac_f32_e32 v99, v140, v140
	v_fmac_f32_e32 v100, v94, v94
	v_add_f32_e32 v99, v99, v100
	v_fmac_f32_e32 v145, 0xba800000, v0
	v_fmac_f32_e32 v143, 0xba800000, v0
	v_add_f32_e32 v98, v98, v99
	v_fmamk_f32 v144, v0, 0xba800000, v144
	v_fmamk_f32 v142, v0, 0xba800000, v142
	v_mul_f32_e32 v99, v143, v143
	v_mul_f32_e32 v100, v145, v145
	v_fmac_f32_e32 v99, v142, v142
	v_fmac_f32_e32 v100, v144, v144
	v_add_f32_e32 v99, v99, v100
	v_fmac_f32_e32 v149, 0xba800000, v0
	v_fmac_f32_e32 v97, 0xba800000, v0
	v_add_f32_e32 v98, v99, v98
	v_fmamk_f32 v148, v0, 0xba800000, v148
	v_fmamk_f32 v96, v0, 0xba800000, v96
	v_mul_f32_e32 v0, v97, v97
	v_mul_f32_e32 v99, v149, v149
	v_fmac_f32_e32 v0, v96, v96
	v_fmac_f32_e32 v99, v148, v148
	v_add_f32_e32 v0, v0, v99
	v_add_f32_e32 v0, v0, v98
	s_nop 1
	v_add_f32_dpp v0, v0, v0 quad_perm:[1,0,3,2] row_mask:0xf bank_mask:0xf
	s_nop 1
	v_add_f32_dpp v0, v0, v0 quad_perm:[2,3,0,1] row_mask:0xf bank_mask:0xf
	s_nop 1
	v_add_f32_dpp v0, v0, v0 row_half_mirror row_mask:0xf bank_mask:0xf
	s_nop 1
	v_add_f32_dpp v0, v0, v0 row_mirror row_mask:0xf bank_mask:0xf
	s_waitcnt lgkmcnt(0)
	v_mov_b32_e32 v98, v0
	s_nop 1
	v_permlane16_swap_b32_e32 v0, v98
	v_add_f32_e32 v0, v0, v98
	v_mov_b32_e32 v98, v0
	s_nop 1
	v_permlane32_swap_b32_e32 v0, v98
	v_add_f32_e32 v0, v0, v98
	v_fmamk_f32 v0, v0, 0x3a800000, v188
	v_cmp_gt_f32_e32 vcc, s31, v0
	v_mul_f32_e32 v98, 0x4f800000, v0
	s_nop 0
	v_cndmask_b32_e32 v0, v0, v98, vcc
	v_sqrt_f32_e32 v98, v0
	s_nop 0
	v_add_u32_e32 v99, -1, v98
	v_fma_f32 v100, -v99, v98, v0
	v_cmp_ge_f32_e64 s[4:5], 0, v100
	v_add_u32_e32 v100, 1, v98
	s_nop 0
	v_cndmask_b32_e64 v99, v98, v99, s[4:5]
	v_fma_f32 v98, -v100, v98, v0
	v_cmp_lt_f32_e64 s[4:5], 0, v98
	s_nop 1
	v_cndmask_b32_e64 v98, v99, v100, s[4:5]
	v_mul_f32_e32 v99, 0x37800000, v98
	v_cndmask_b32_e32 v98, v98, v99, vcc
	v_cmp_class_f32_e32 vcc, v0, v189
	s_nop 1
	v_cndmask_b32_e32 v0, v98, v0, vcc
	v_div_scale_f32 v98, s[0:1], v0, v0, 1.0
	v_rcp_f32_e32 v99, v98
	s_mov_b64 s[0:1], -1
	v_fma_f32 v100, -v98, v99, 1.0
	v_fmac_f32_e32 v99, v100, v99
	v_div_scale_f32 v100, vcc, 1.0, v0, 1.0
	v_mul_f32_e32 v101, v100, v99
	v_fma_f32 v102, -v98, v101, v100
	v_fmac_f32_e32 v101, v102, v99
	v_fma_f32 v98, -v98, v101, v100
	v_div_fmas_f32 v98, v98, v99, v101
	v_div_fixup_f32 v0, v98, v0, 1.0
	v_pk_mul_f32 v[92:93], v[92:93], v[0:1] op_sel_hi:[1,0]
	v_pk_mul_f32 v[90:91], v[90:91], v[0:1] op_sel_hi:[1,0]
	v_pk_fma_f32 v[98:99], v[2:3], v[92:93], v[6:7]
	v_pk_fma_f32 v[100:101], v[4:5], v[90:91], v[8:9]
	v_pk_mul_f32 v[90:91], v[140:141], v[0:1] op_sel_hi:[1,0]
	v_pk_mul_f32 v[92:93], v[94:95], v[0:1] op_sel_hi:[1,0]
	v_pk_fma_f32 v[102:103], v[10:11], v[90:91], v[14:15]
	v_pk_fma_f32 v[104:105], v[12:13], v[92:93], v[16:17]
	v_pk_mul_f32 v[90:91], v[142:143], v[0:1] op_sel_hi:[1,0]
	v_pk_mul_f32 v[92:93], v[144:145], v[0:1] op_sel_hi:[1,0]
	v_pk_mul_f32 v[94:95], v[96:97], v[0:1] op_sel_hi:[1,0]
	v_pk_mul_f32 v[96:97], v[148:149], v[0:1] op_sel_hi:[1,0]
	v_pk_fma_f32 v[92:93], v[20:21], v[92:93], v[24:25]
	v_pk_fma_f32 v[90:91], v[18:19], v[90:91], v[22:23]
	v_pk_fma_f32 v[96:97], v[28:29], v[96:97], v[32:33]
	v_pk_fma_f32 v[94:95], v[26:27], v[94:95], v[30:31]
	s_waitcnt vmcnt(0)
	s_and_b64 vcc, exec, s[2:3]
	s_cbranch_vccnz .LBB0_1212
	v_bfe_u32 v0, v98, 16, 1
	v_add3_u32 v0, v98, v0, s43
	v_bfe_u32 v107, v99, 16, 1
	v_lshrrev_b32_e32 v0, 16, v0
	v_add3_u32 v107, v99, v107, s43
	v_and_or_b32 v140, v107, s33, v0
	v_bfe_u32 v0, v100, 16, 1
	v_add3_u32 v0, v100, v0, s43
	v_bfe_u32 v107, v101, 16, 1
	v_lshrrev_b32_e32 v0, 16, v0
	v_add3_u32 v107, v101, v107, s43
	v_and_or_b32 v141, v107, s33, v0
	v_bfe_u32 v0, v102, 16, 1
	v_add3_u32 v0, v102, v0, s43
	v_bfe_u32 v107, v103, 16, 1
	v_lshrrev_b32_e32 v0, 16, v0
	v_add3_u32 v107, v103, v107, s43
	v_and_or_b32 v142, v107, s33, v0
	v_bfe_u32 v0, v104, 16, 1
	v_add3_u32 v0, v104, v0, s43
	v_bfe_u32 v107, v105, 16, 1
	v_lshrrev_b32_e32 v0, 16, v0
	v_add3_u32 v107, v105, v107, s43
	v_and_or_b32 v143, v107, s33, v0
	v_bfe_u32 v0, v90, 16, 1
	v_add_co_u32_e32 v144, vcc, s39, v138
	v_add3_u32 v0, v90, v0, s43
	v_bfe_u32 v107, v91, 16, 1
	v_addc_co_u32_e32 v145, vcc, 0, v139, vcc
	v_lshrrev_b32_e32 v0, 16, v0
	v_add3_u32 v107, v91, v107, s43
	global_store_dwordx4 v[144:145], v[140:143], off
	s_mov_b64 s[0:1], 0
	s_nop 0
	v_and_or_b32 v140, v107, s33, v0
	v_bfe_u32 v0, v92, 16, 1
	v_add3_u32 v0, v92, v0, s43
	v_bfe_u32 v107, v93, 16, 1
	v_lshrrev_b32_e32 v0, 16, v0
	v_add3_u32 v107, v93, v107, s43
	v_and_or_b32 v141, v107, s33, v0
	v_bfe_u32 v0, v94, 16, 1
	v_add3_u32 v0, v94, v0, s43
	v_bfe_u32 v107, v95, 16, 1
	v_lshrrev_b32_e32 v0, 16, v0
	v_add3_u32 v107, v95, v107, s43
	v_and_or_b32 v142, v107, s33, v0
	v_bfe_u32 v0, v96, 16, 1
	v_add3_u32 v0, v96, v0, s43
	v_bfe_u32 v107, v97, 16, 1
	v_lshrrev_b32_e32 v0, 16, v0
	v_add3_u32 v107, v97, v107, s43
	v_and_or_b32 v143, v107, s33, v0
	global_store_dwordx4 v[144:145], v[140:143], off offset:1024
